# interleaved RWKV scan chains, RWKV prep wave 4 active again, retention prep first-iteration waits removed, retention scan ready-flag read hoisted
# speedup vs baseline: 1.0126x; 1.0092x over previous
.LBB0_934:
	v_mov_b32_e32 v75, v74
	v_pk_mul_f32 v[72:73], v[74:75], v[72:73]
	v_pk_mul_f32 v[70:71], v[78:79], v[70:71]
	v_pk_mul_f32 v[68:69], v[74:75], v[68:69]
	v_pk_mul_f32 v[66:67], v[78:79], v[66:67]
	v_cvt_pk_bf16_f32 v80, v70, v71
	v_cvt_pk_bf16_f32 v81, v72, v73
	v_cvt_pk_bf16_f32 v82, v66, v67
	v_cvt_pk_bf16_f32 v83, v68, v69
	v_pk_mul_f32 v[64:65], v[74:75], v[64:65]
	v_pk_mul_f32 v[62:63], v[78:79], v[62:63]
	s_waitcnt lgkmcnt(7)
	v_mfma_f32_16x16x32_bf16 v[80:83], v[36:39], v[80:83], 0
	v_mul_f32_e64 v60, v74, v60
	v_mul_f32_e64 v61, v75, v61
	v_pk_mul_f32 v[58:59], v[78:79], v[58:59]
	v_cvt_pk_bf16_f32 v84, v62, v63
	v_cvt_pk_bf16_f32 v85, v64, v65
	v_cvt_pk_bf16_f32 v86, v58, v59
	v_cvt_pk_bf16_f32 v87, v60, v61
	v_mov_b32_e32 v28, v129
	v_mov_b32_e32 v29, v129
	s_waitcnt lgkmcnt(6)
	v_mfma_f32_16x16x32_bf16 v[32:35], v[32:35], v[84:87], v[80:83]
	v_mov_b32_e32 v50, v129
	v_mov_b32_e32 v51, v129
	v_mov_b32_e32 v46, v129
	v_mov_b32_e32 v47, v129
	v_mov_b32_e32 v54, v129
	v_mov_b32_e32 v55, v129
	v_mov_b32_e32 v38, v129
	v_mov_b32_e32 v39, v129
	s_lshl_b32 s92, s9, 15
	v_lshl_add_u64 v[12:13], v[76:77], 0, s[92:93]
	s_waitcnt lgkmcnt(4)
	v_mfma_f32_16x16x32_bf16 v[32:35], v[42:45], v[38:41], v[32:35]
	s_mov_b32 s30, s8
	s_or_b32 s100, s30, 1
	s_mul_i32 s101, s100, 0xcd
	s_bfe_u32 s101, s101, 0x5000b
	s_mul_i32 s101, s101, 10
	s_sub_i32 s100, s100, s101
	s_and_b32 s100, s100, 0xff
	s_lshl_b32 s100, s100, 2
	s_add_i32 s100, s100, 0x1fa00
	v_mov_b32_e32 v140, s100
	ds_read_b32 v140, v140
	s_waitcnt lgkmcnt(4)
	v_mfma_f32_16x16x32_bf16 v[28:31], v[28:31], v[38:41], v[70:73]
	s_waitcnt lgkmcnt(3)
	v_mfma_f32_16x16x32_bf16 v[50:53], v[50:53], v[38:41], v[66:69]
	s_nop 2
	v_cvt_pk_bf16_f32 v16, v32, v33
	global_store_short v[12:13], v16, off offset:1024
	global_store_short_d16_hi v[12:13], v16, off offset:3072
	v_add_co_u32_e32 v12, vcc, s7, v12
	s_waitcnt lgkmcnt(2)
	v_mfma_f32_16x16x32_bf16 v[46:49], v[46:49], v[38:41], v[62:65]
	v_addc_co_u32_e32 v13, vcc, 0, v13, vcc
	v_pk_mul_f32 v[30:31], v[74:75], v[30:31]
	s_waitcnt lgkmcnt(1)
	v_mfma_f32_16x16x32_bf16 v[54:57], v[54:57], v[38:41], v[58:61]
	v_mul_f32_e64 v28, v78, v28
	v_mul_f32_e64 v29, v79, v29
	v_pk_mul_f32 v[52:53], v[74:75], v[52:53]
	v_pk_mul_f32 v[50:51], v[78:79], v[50:51]
	v_pk_mul_f32 v[48:49], v[74:75], v[48:49]
	v_pk_mul_f32 v[46:47], v[78:79], v[46:47]
	s_nop 1
	v_pk_mul_f32 v[56:57], v[74:75], v[56:57]
	v_pk_mul_f32 v[54:55], v[78:79], v[54:55]
	v_cvt_pk_bf16_f32 v17, v34, v35
	s_and_b64 vcc, exec, s[26:27]
	global_store_short v[12:13], v17, off offset:1024
	global_store_short_d16_hi v[12:13], v17, off offset:3072
	s_cbranch_vccnz .LBB0_956

.LBB0_937:
	s_or_b64 exec, exec, s[26:27]
	s_mul_i32 s8, s9, 0xcd
	s_bfe_u32 s8, s8, 0x5000b
	s_mul_i32 s8, s8, 10
	s_sub_i32 s8, s9, s8
	s_and_b32 s21, s8, 0xff
	s_lshl_b32 s8, s21, 2
	s_add_i32 s31, s8, 0
	s_add_i32 s31, s31, 0x1fa00
	s_add_i32 s8, s30, 2
	s_mov_b32 s73, 0x400001
	v_cmp_eq_u32_e32 vcc, s8, v140
	s_cbranch_vccnz .LBB0_945
	s_branch .LBB0_939

.LBB0_945:
	v_cvt_pk_bf16_f32 v40, v28, v29
	v_cvt_pk_bf16_f32 v41, v30, v31
	v_cvt_pk_bf16_f32 v42, v50, v51
	v_cvt_pk_bf16_f32 v43, v52, v53
	s_mulk_i32 s21, 0x3200
	s_add_i32 s21, s21, 0
	v_mfma_f32_16x16x32_bf16 v[40:43], v[0:3], v[40:43], 0
	v_add3_u32 v12, s21, v194, v203
	v_cvt_pk_bf16_f32 v58, v46, v47
	v_cvt_pk_bf16_f32 v59, v48, v49
	v_cvt_pk_bf16_f32 v60, v54, v55
	v_cvt_pk_bf16_f32 v61, v56, v57
	v_add_u32_e32 v12, 0x800, v12
	ds_read2_b64 v[36:39], v12 offset1:4
	ds_read2_b64 v[32:35], v12 offset0:8 offset1:12
	v_mfma_f32_16x16x32_bf16 v[80:83], v[4:7], v[58:61], v[40:43]
	v_mov_b32_e32 v12, v129
	v_mov_b32_e32 v13, v129
	v_mov_b32_e32 v16, v129
	v_mov_b32_e32 v17, v129
	v_mov_b32_e32 v128, v129
	v_mov_b32_e32 v20, v129
	v_mov_b32_e32 v21, v129
	v_mov_b32_e32 v24, v129
	v_mov_b32_e32 v25, v129
	v_mfma_f32_16x16x32_bf16 v[80:83], v[8:11], v[128:131], v[80:83]
	s_lshl_b32 s92, s30, 15
	s_mul_i32 s101, s8, 0xcd
	s_bfe_u32 s101, s101, 0x5000b
	s_mul_i32 s101, s101, 10
	s_sub_i32 s100, s8, s101
	s_and_b32 s100, s100, 0xff
	s_lshl_b32 s100, s100, 2
	s_add_i32 s100, s100, 0x1fa00
	v_mov_b32_e32 v141, s100
	ds_read_b32 v141, v141
	v_mfma_f32_16x16x32_bf16 v[70:73], v[12:15], v[128:131], v[28:31]
	v_add3_u32 v12, s21, v204, v191
	v_add_u32_e32 v13, s20, v12
	v_mfma_f32_16x16x32_bf16 v[66:69], v[16:19], v[128:131], v[50:53]
	v_add3_u32 v16, s21, v196, v195
	ds_read_b64_tr_b16 v[40:41], v13 offset:10496
	ds_read_b128 v[42:45], v16 offset:9216
	v_cvt_pk_bf16_f32 v16, v80, v81
	v_mfma_f32_16x16x32_bf16 v[62:65], v[20:23], v[128:131], v[46:49]
	v_cvt_pk_bf16_f32 v17, v82, v83
	v_mfma_f32_16x16x32_bf16 v[58:61], v[24:27], v[128:131], v[54:57]
	ds_read_b64_tr_b16 v[30:31], v12 offset:6144
	ds_read_b64_tr_b16 v[52:53], v12 offset:6176
	ds_read_b64_tr_b16 v[48:49], v12 offset:6208
	ds_read_b64_tr_b16 v[56:57], v12 offset:6240
	v_lshl_add_u64 v[12:13], v[76:77], 0, s[92:93]
	global_store_short v[12:13], v16, off offset:1024
	global_store_short_d16_hi v[12:13], v16, off offset:3072
	v_add_co_u32_e32 v12, vcc, 0x1000, v12
	s_nop 1
	v_addc_co_u32_e32 v13, vcc, 0, v13, vcc
	global_store_short v[12:13], v17, off offset:1024
	global_store_short_d16_hi v[12:13], v17, off offset:3072
	s_waitcnt lgkmcnt(0)
	s_and_saveexec_b64 s[26:27], s[36:37]
	s_cbranch_execz .LBB0_947
	v_readlane_b32 s21, v254, 3
	v_mov_b32_e32 v13, s8
	s_nop 0
	v_mov_b32_e32 v12, s21
	ds_write_b32 v12, v13 offset:48
.LBB0_947:
	s_or_b64 exec, exec, s[26:27]
	s_cmpk_gt_u32 s30, 0xfd
	s_cselect_b64 s[26:27], -1, 0
	s_and_b64 vcc, exec, s[26:27]
	s_cbranch_vccnz .LBB0_934
	s_mul_i32 s21, s8, 0xcd
	s_bfe_u32 s21, s21, 0x5000b
	s_mul_i32 s21, s21, 10
	s_sub_i32 s21, s8, s21
	s_and_b32 s21, s21, 0xff
	s_lshl_b32 s31, s21, 2
	s_add_i32 s73, s31, 0
	s_add_i32 s73, s73, 0x1fa00
	s_add_i32 s76, s30, 3
	s_mov_b32 s77, 0x400001
	v_cmp_eq_u32_e32 vcc, s76, v141
	s_cbranch_vccnz .LBB0_933
	s_branch .LBB0_950
